# fused MoE unit scheduler: expert lookup reuses the current unit's expert when the row tile is unchanged and otherwise resumes the LDS search from it (was a from-zero linear LDS search before every uni
# speedup vs baseline: 1.0185x; 1.0095x over previous
; __device__ __forceinline__ int moe_expert_of(const LAS int* tb, int rt) { int e = 0; while (tb[e + 1] <= rt) ++e; return e; }
;     __device__ __forceinline__ bool next(int i, gm::GUnit& u) const {
;         const int ti = i / 12, s = i % 12, rt = ti * G + c;
;         if (rt >= nfull) return false;
;         const int e = moe_expert_of(tb, rt);
.LBB0_1779:
	s_add_i32 s40, s40, 1
	s_mul_hi_u32 s22, s40, 0xaaaaaaab
	s_lshr_b32 s29, s22, 3
	s_mul_i32 s22, s29, s96
	s_add_i32 s28, s22, s28
	s_cmp_lt_i32 s28, s64
	s_cselect_b64 s[22:23], -1, 0
	s_cmp_ge_i32 s28, s64
	s_cselect_b64 s[56:57], -1, 0
	s_and_b64 vcc, exec, s[56:57]
	s_cbranch_vccnz .LBB0_1787
	s_cmp_lg_u32 s28, s92
	s_cbranch_scc1 .Lmoe_f_search
	s_mov_b32 s76, s62
	s_branch .Lmoe_f_found
.Lmoe_f_search:
	s_lshl_b32 s30, s62, 2
	s_add_i32 s30, s30, 0x23044
	s_add_i32 s76, s62, -1

;     __device__ __forceinline__ bf16_t* H() const { return (bf16_t*)(ws + WS_H); }
;     __device__ __forceinline__ bf16_t* act() const { return (bf16_t*)(ws + WS_PROJ); }
;     __device__ __forceinline__ int* rtok() const { return (int*)(ws + WS_RTOK); }
; __device__ __forceinline__ int moe_expert_of(const LAS int* tb, int rt) { int e = 0; while (tb[e + 1] <= rt) ++e; return e; }
;     __device__ __forceinline__ bool next(int i, gm::GUnit& u) const {
;         const int ti = i / 12, s = i % 12, rt = ti * G + c;
;         if (rt >= nfull) return false;
;         const int e = moe_expert_of(tb, rt);
;         u.pm = rt; u.sub = s; u.e = e; u.lda = 2048; u.ldb = 2048; u.nt = 16; u.aux = aux;
;         if (s < 8) { u.pn = s; u.A = H; u.gidx = rtok + (size_t)rt * 256; u.B = GU + ((size_t)e * 2048 + s * 256) * 2048; }
;         else { u.pn = s - 8; u.A = act + aux; u.gidx = nullptr; u.B = DN + ((size_t)e * 1024 + (s - 8) * 256) * 2048; }
;         return true;
.Lmoe_f_found:
	s_mul_i32 s29, s29, 12
	s_sub_i32 s41, s40, s29
	s_cmp_gt_u32 s41, 7
	s_mov_b64 s[30:31], -1
	s_cbranch_scc0 .LBB0_1784
	s_add_i32 s79, s41, -8
	s_lshl_b32 s30, s79, 8
	s_mov_b32 s31, s77
	s_lshl_b64 s[52:53], s[76:77], 21
	s_lshl_b64 s[30:31], s[30:31], 11
	s_add_u32 s29, s58, s52
	s_addc_u32 s52, s59, s53
	s_add_u32 s54, s29, s30
	s_addc_u32 s55, s52, s31
	s_mov_b64 s[30:31], 0
